# prep phase: both rows' loads in flight together (row-1 rope-key conversion deferred to the common wait)
# speedup vs baseline: 1.0057x; 1.0057x over previous
; __device__ __forceinline__ void prep_phase(const Frame& F, const bf16_t* __restrict__ PROJ, const float* __restrict__ qn, const float* __restrict__ kvn, const f32x2* __restrict__ CS, bf16_t* __restrict__ CQN, bf16_t* __restrict__ CKVN, bf16_t* __restrict__ KB, float* __restrict__ KM) {
;     ...
;     auto prep_load = [&](int row, u32x4& a, u32x4& b, float& x1, float& x2, f32x2& cs) {
;         const bf16_t* p = PROJ + (size_t)row * INCP;
;         a = (u32x4){0u, 0u, 0u, 0u}; b = (u32x4){0u, 0u, 0u, 0u}; x1 = 0.f; x2 = 0.f; cs = (f32x2){0.f, 0.f};
;         if (lane < 48) a = *(const u32x4*)(p + C_CQ + lane * 8);
;         if (lane < 32) b = *(const u32x4*)(p + C_CKV + lane * 8);
;         if (lane < 16) { x1 = bf2f(p[C_KR + lane]); x2 = bf2f(p[C_KR + 16 + lane]); cs = CS[(size_t)(row % SEQ) * 16 + lane]; }
.LBB0_315:
	s_or_b64 exec, exec, s[18:19]
	v_mov_b32_e32 v14, 0
	v_mov_b32_e32 v60, 0
	s_waitcnt lgkmcnt(0)
	v_mov_b32_e32 v61, 0
	v_mov_b32_e32 v62, 0
	v_mov_b32_e32 v63, 0
	v_mov_b32_e32 v148, 0
	v_mov_b32_e32 v149, 0
	s_and_saveexec_b64 s[18:19], s[6:7]
	s_cbranch_execz .LBB0_317
	s_ashr_i32 s20, s28, 31
	s_lshr_b32 s20, s20, 19
	s_add_i32 s20, s28, s20
	s_and_b32 s20, s20, 0xffffe000
	s_sub_i32 s20, s28, s20
	s_ashr_i32 s21, s20, 31
	v_lshl_add_u64 v[16:17], s[90:91], 0, v[54:55]
	s_lshl_b64 s[20:21], s[20:21], 7
	v_add_co_u32_e32 v16, vcc, 0x3b341000, v16
	v_lshl_add_u64 v[18:19], v[38:39], 0, s[20:21]
	s_nop 0
	v_addc_co_u32_e32 v17, vcc, 0, v17, vcc
	global_load_dwordx2 v[60:61], v[18:19], off
	global_load_ushort v148, v[16:17], off offset:256
	s_nop 0
	global_load_ushort v149, v[16:17], off offset:288

; __device__ __forceinline__ unsigned pk2(float lo, float hi) { return f2bf(lo) | (f2bf(hi) << 16); }
; __device__ __forceinline__ void prep_phase(const Frame& F, const bf16_t* __restrict__ PROJ, const float* __restrict__ qn, const float* __restrict__ kvn, const f32x2* __restrict__ CS, bf16_t* __restrict__ CQN, bf16_t* __restrict__ CKVN, bf16_t* __restrict__ KB, float* __restrict__ KM) {
;     ...
;     auto prep_finish = [&](int row, const u32x4 a, const u32x4 b, float x1, float x2, f32x2 cs, const f32x4 gq0, const f32x4 gq1, const f32x4 gk0, const f32x4 gk1) {
;         float sq = 0.f, sk = 0.f;
; #pragma unroll
;         for (int i = 0; i < 4; ++i) { const float x = bflo(a[i]), y = bfhi(a[i]), z = bflo(b[i]), w = bfhi(b[i]); sq += x * x + y * y; sk += z * z + w * w; }
;         sq = wave_sum(sq); sk = wave_sum(sk);
;         const float rq = rsqrtf(sq * (1.f / QL) + RMS_EPS), rk = rsqrtf(sk * (1.f / KVL) + RMS_EPS);
;         if (lane < 48) { u32x4 o;
;             o.x = pk2(bflo(a.x) * rq * gq0[0], bfhi(a.x) * rq * gq0[1]); o.y = pk2(bflo(a.y) * rq * gq0[2], bfhi(a.y) * rq * gq0[3]);
;             o.z = pk2(bflo(a.z) * rq * gq1[0], bfhi(a.z) * rq * gq1[1]); o.w = pk2(bflo(a.w) * rq * gq1[2], bfhi(a.w) * rq * gq1[3]);
;             *(u32x4*)(CQN + (size_t)row * QL + lane * 8) = o; }
.LBB0_323:
	s_or_b64 exec, exec, s[24:25]
	s_waitcnt vmcnt(0)
	v_lshlrev_b32_e32 v62, 16, v148
	v_lshlrev_b32_e32 v63, 16, v149
	v_and_b32_e32 v67, 0xffff0000, v27
	v_and_b32_e32 v66, 0xffff0000, v26
	v_lshlrev_b32_e32 v65, 16, v27
	v_lshlrev_b32_e32 v64, 16, v26
	v_pk_mul_f32 v[26:27], v[66:67], v[66:67]
	v_and_b32_e32 v71, 0xffff0000, v29
	v_pk_fma_f32 v[80:81], v[64:65], v[64:65], v[26:27]
	v_lshlrev_b32_e32 v27, 16, v23
	v_lshlrev_b32_e32 v26, 16, v22
	v_and_b32_e32 v23, 0xffff0000, v23
	v_and_b32_e32 v22, 0xffff0000, v22
	v_pk_mul_f32 v[68:69], v[22:23], v[22:23]
	v_and_b32_e32 v70, 0xffff0000, v28
	v_pk_fma_f32 v[82:83], v[26:27], v[26:27], v[68:69]
	v_lshlrev_b32_e32 v69, 16, v29
	v_lshlrev_b32_e32 v68, 16, v28
	v_pk_mul_f32 v[28:29], v[70:71], v[70:71]
	v_add_f32_e32 v80, v80, v81
	v_pk_fma_f32 v[84:85], v[68:69], v[68:69], v[28:29]
	v_lshlrev_b32_e32 v29, 16, v25
	v_lshlrev_b32_e32 v28, 16, v24
	v_and_b32_e32 v25, 0xffff0000, v25
	v_and_b32_e32 v24, 0xffff0000, v24
	v_add_f32_e32 v80, v84, v80
	v_add_f32_e32 v84, v85, v80
	v_pk_mul_f32 v[80:81], v[24:25], v[24:25]
	v_add_f32_e32 v82, v82, v83
	v_pk_fma_f32 v[80:81], v[28:29], v[28:29], v[80:81]
	s_nop 0
	v_add_f32_e32 v80, v80, v82
	v_add_f32_e32 v80, v81, v80
	ds_bpermute_b32 v82, v1, v84
	ds_bpermute_b32 v81, v1, v80
	s_waitcnt lgkmcnt(0)
	v_add_f32_e32 v82, v84, v82
	v_add_f32_e32 v80, v80, v81
	ds_bpermute_b32 v83, v72, v82
	ds_bpermute_b32 v81, v72, v80
	s_waitcnt lgkmcnt(1)
	v_add_f32_e32 v82, v82, v83
	s_waitcnt lgkmcnt(0)
	v_add_f32_e32 v80, v80, v81
	ds_bpermute_b32 v83, v73, v82
	ds_bpermute_b32 v81, v73, v80
	s_waitcnt lgkmcnt(1)
	v_add_f32_e32 v82, v82, v83
	s_waitcnt lgkmcnt(0)
	v_add_f32_e32 v80, v80, v81
	ds_bpermute_b32 v83, v74, v82
	ds_bpermute_b32 v81, v74, v80
	s_waitcnt lgkmcnt(1)
	v_add_f32_e32 v82, v82, v83
	s_waitcnt lgkmcnt(0)
	v_add_f32_e32 v80, v80, v81
	ds_bpermute_b32 v83, v75, v82
	ds_bpermute_b32 v81, v75, v80
	s_waitcnt lgkmcnt(1)
	v_add_f32_e32 v82, v82, v83
	s_waitcnt lgkmcnt(0)
	v_add_f32_e32 v80, v80, v81
	ds_bpermute_b32 v83, v76, v82
	ds_bpermute_b32 v81, v76, v80
	s_and_saveexec_b64 s[22:23], s[0:1]
	s_cbranch_execz .LBB0_327
	s_waitcnt lgkmcnt(1)
	v_add_f32_e32 v82, v82, v83
	v_fmamk_f32 v82, v82, 0x3b2aaaab, v79
	v_mul_f32_e32 v83, 0x4b800000, v82
	v_cmp_gt_f32_e32 vcc, s26, v82
	s_nop 1
	v_cndmask_b32_e32 v82, v82, v83, vcc
	v_rsq_f32_e32 v82, v82
	s_nop 0
	v_mul_f32_e32 v83, 0x45800000, v82
	v_cndmask_b32_e32 v82, v82, v83, vcc
	v_pk_mul_f32 v[66:67], v[82:83], v[66:67] op_sel_hi:[0,1]
	v_pk_mul_f32 v[70:71], v[82:83], v[70:71] op_sel_hi:[0,1]
	v_pk_mul_f32 v[64:65], v[82:83], v[64:65] op_sel_hi:[0,1]
	v_pk_mul_f32 v[66:67], v[8:9], v[66:67]
	v_pk_mul_f32 v[68:69], v[82:83], v[68:69] op_sel_hi:[0,1]
	v_pk_mul_f32 v[70:71], v[34:35], v[70:71]
	v_pk_mul_f32 v[64:65], v[10:11], v[64:65]
	v_pk_mul_f32 v[68:69], v[6:7], v[68:69]
	v_bfe_u32 v82, v71, 16, 1
	v_bfe_u32 v83, v70, 16, 1
	v_bfe_u32 v84, v67, 16, 1
	v_bfe_u32 v85, v66, 16, 1
	v_add3_u32 v85, v66, v85, s27
	v_add3_u32 v84, v67, v84, s27
	v_add3_u32 v66, v70, v83, s27
	v_add3_u32 v67, v71, v82, s27
	v_bfe_u32 v70, v64, 16, 1
	v_bfe_u32 v71, v65, 16, 1
	v_bfe_u32 v82, v68, 16, 1
	v_bfe_u32 v83, v69, 16, 1
	v_add3_u32 v69, v69, v83, s27
	v_add3_u32 v68, v68, v82, s27
	v_add3_u32 v65, v65, v71, s27
	v_add3_u32 v64, v64, v70, s27
	v_lshrrev_b32_e32 v64, 16, v64
	v_lshrrev_b32_e32 v65, 16, v65
	v_lshrrev_b32_e32 v68, 16, v68
	v_lshrrev_b32_e32 v69, 16, v69
	v_and_or_b32 v67, v67, s9, v69
	v_and_or_b32 v66, v66, s9, v68
	v_and_or_b32 v65, v84, s9, v65
	v_and_or_b32 v64, v85, s9, v64
	v_lshl_add_u64 v[68:69], s[90:91], 0, v[46:47]
	global_store_dwordx4 v[68:69], v[64:67], off
	s_or_b64 exec, exec, s[22:23]
	s_and_saveexec_b64 s[22:23], s[4:5]
	s_cbranch_execnz .LBB0_328

; __device__ __forceinline__ void prep_phase(const Frame& F, const bf16_t* __restrict__ PROJ, const float* __restrict__ qn, const float* __restrict__ kvn, const f32x2* __restrict__ CS, bf16_t* __restrict__ CQN, bf16_t* __restrict__ CKVN, bf16_t* __restrict__ KB, float* __restrict__ KM) {
;     ...
;     auto prep_load = [&](int row, u32x4& a, u32x4& b, float& x1, float& x2, f32x2& cs) {
;         const bf16_t* p = PROJ + (size_t)row * INCP;
;         a = (u32x4){0u, 0u, 0u, 0u}; b = (u32x4){0u, 0u, 0u, 0u}; x1 = 0.f; x2 = 0.f; cs = (f32x2){0.f, 0.f};
;         if (lane < 48) a = *(const u32x4*)(p + C_CQ + lane * 8);
;         if (lane < 32) b = *(const u32x4*)(p + C_CKV + lane * 8);
;         if (lane < 16) { x1 = bf2f(p[C_KR + lane]); x2 = bf2f(p[C_KR + 16 + lane]); cs = CS[(size_t)(row % SEQ) * 16 + lane]; }
.LBB0_2774:
	s_or_b64 exec, exec, s[18:19]
	v_mov_b32_e32 v14, 0
	v_mov_b32_e32 v60, 0
	s_waitcnt lgkmcnt(0)
	v_mov_b32_e32 v61, 0
	v_mov_b32_e32 v62, 0
	v_mov_b32_e32 v63, 0
	v_mov_b32_e32 v120, 0
	v_mov_b32_e32 v121, 0
	s_and_saveexec_b64 s[18:19], s[6:7]
	s_cbranch_execz .LBB0_2776
	s_ashr_i32 s20, s28, 31
	s_lshr_b32 s20, s20, 19
	s_add_i32 s20, s28, s20
	s_and_b32 s20, s20, 0xffffe000
	v_lshl_add_u64 v[16:17], s[90:91], 0, v[54:55]
	s_sub_i32 s20, s28, s20
	v_add_co_u32_e32 v16, vcc, 0x3b341000, v16
	s_ashr_i32 s21, s20, 31
	s_nop 0
	v_addc_co_u32_e32 v17, vcc, 0, v17, vcc
	s_lshl_b64 s[20:21], s[20:21], 7
	v_lshl_add_u64 v[18:19], v[38:39], 0, s[20:21]
	global_load_ushort v120, v[16:17], off offset:256
	s_nop 0
	global_load_ushort v121, v[16:17], off offset:288
	s_nop 0
	global_load_dwordx2 v[60:61], v[18:19], off

; __device__ __forceinline__ unsigned pk2(float lo, float hi) { return f2bf(lo) | (f2bf(hi) << 16); }
; __device__ __forceinline__ void prep_phase(const Frame& F, const bf16_t* __restrict__ PROJ, const float* __restrict__ qn, const float* __restrict__ kvn, const f32x2* __restrict__ CS, bf16_t* __restrict__ CQN, bf16_t* __restrict__ CKVN, bf16_t* __restrict__ KB, float* __restrict__ KM) {
;     ...
;     auto prep_finish = [&](int row, const u32x4 a, const u32x4 b, float x1, float x2, f32x2 cs, const f32x4 gq0, const f32x4 gq1, const f32x4 gk0, const f32x4 gk1) {
;         float sq = 0.f, sk = 0.f;
; #pragma unroll
;         for (int i = 0; i < 4; ++i) { const float x = bflo(a[i]), y = bfhi(a[i]), z = bflo(b[i]), w = bfhi(b[i]); sq += x * x + y * y; sk += z * z + w * w; }
;         sq = wave_sum(sq); sk = wave_sum(sk);
;         const float rq = rsqrtf(sq * (1.f / QL) + RMS_EPS), rk = rsqrtf(sk * (1.f / KVL) + RMS_EPS);
;         if (lane < 48) { u32x4 o;
;             o.x = pk2(bflo(a.x) * rq * gq0[0], bfhi(a.x) * rq * gq0[1]); o.y = pk2(bflo(a.y) * rq * gq0[2], bfhi(a.y) * rq * gq0[3]);
;             o.z = pk2(bflo(a.z) * rq * gq1[0], bfhi(a.z) * rq * gq1[1]); o.w = pk2(bflo(a.w) * rq * gq1[2], bfhi(a.w) * rq * gq1[3]);
;             *(u32x4*)(CQN + (size_t)row * QL + lane * 8) = o; }
.LBB0_2782:
	s_or_b64 exec, exec, s[24:25]
	s_waitcnt vmcnt(0)
	v_lshlrev_b32_e32 v62, 16, v120
	v_lshlrev_b32_e32 v63, 16, v121
	v_and_b32_e32 v67, 0xffff0000, v27
	v_and_b32_e32 v66, 0xffff0000, v26
	v_lshlrev_b32_e32 v65, 16, v27
	v_lshlrev_b32_e32 v64, 16, v26
	v_pk_mul_f32 v[26:27], v[66:67], v[66:67]
	v_and_b32_e32 v71, 0xffff0000, v29
	v_pk_fma_f32 v[80:81], v[64:65], v[64:65], v[26:27]
	v_lshlrev_b32_e32 v27, 16, v23
	v_lshlrev_b32_e32 v26, 16, v22
	v_and_b32_e32 v23, 0xffff0000, v23
	v_and_b32_e32 v22, 0xffff0000, v22
	v_pk_mul_f32 v[68:69], v[22:23], v[22:23]
	v_and_b32_e32 v70, 0xffff0000, v28
	v_pk_fma_f32 v[82:83], v[26:27], v[26:27], v[68:69]
	v_lshlrev_b32_e32 v69, 16, v29
	v_lshlrev_b32_e32 v68, 16, v28
	v_pk_mul_f32 v[28:29], v[70:71], v[70:71]
	v_add_f32_e32 v80, v80, v81
	v_pk_fma_f32 v[84:85], v[68:69], v[68:69], v[28:29]
	v_lshlrev_b32_e32 v29, 16, v25
	v_lshlrev_b32_e32 v28, 16, v24
	v_and_b32_e32 v25, 0xffff0000, v25
	v_and_b32_e32 v24, 0xffff0000, v24
	v_add_f32_e32 v80, v84, v80
	v_add_f32_e32 v84, v85, v80
	v_pk_mul_f32 v[80:81], v[24:25], v[24:25]
	v_add_f32_e32 v82, v82, v83
	v_pk_fma_f32 v[80:81], v[28:29], v[28:29], v[80:81]
	s_nop 0
	v_add_f32_e32 v80, v80, v82
	v_add_f32_e32 v80, v81, v80
	ds_bpermute_b32 v82, v1, v84
	ds_bpermute_b32 v81, v1, v80
	s_waitcnt lgkmcnt(0)
	v_add_f32_e32 v82, v84, v82
	v_add_f32_e32 v80, v80, v81
	ds_bpermute_b32 v83, v72, v82
	ds_bpermute_b32 v81, v72, v80
	s_waitcnt lgkmcnt(1)
	v_add_f32_e32 v82, v82, v83
	s_waitcnt lgkmcnt(0)
	v_add_f32_e32 v80, v80, v81
	ds_bpermute_b32 v83, v73, v82
	ds_bpermute_b32 v81, v73, v80
	s_waitcnt lgkmcnt(1)
	v_add_f32_e32 v82, v82, v83
	s_waitcnt lgkmcnt(0)
	v_add_f32_e32 v80, v80, v81
	ds_bpermute_b32 v83, v74, v82
	ds_bpermute_b32 v81, v74, v80
	s_waitcnt lgkmcnt(1)
	v_add_f32_e32 v82, v82, v83
	s_waitcnt lgkmcnt(0)
	v_add_f32_e32 v80, v80, v81
	ds_bpermute_b32 v83, v75, v82
	ds_bpermute_b32 v81, v75, v80
	s_waitcnt lgkmcnt(1)
	v_add_f32_e32 v82, v82, v83
	s_waitcnt lgkmcnt(0)
	v_add_f32_e32 v80, v80, v81
	ds_bpermute_b32 v83, v76, v82
	ds_bpermute_b32 v81, v76, v80
	s_and_saveexec_b64 s[22:23], s[0:1]
	s_cbranch_execz .LBB0_2786
	s_waitcnt lgkmcnt(1)
	v_add_f32_e32 v82, v82, v83
	v_fmamk_f32 v82, v82, 0x3b2aaaab, v79
	v_mul_f32_e32 v83, 0x4b800000, v82
	v_cmp_gt_f32_e32 vcc, s26, v82
	s_nop 1
	v_cndmask_b32_e32 v82, v82, v83, vcc
	v_rsq_f32_e32 v82, v82
	s_nop 0
	v_mul_f32_e32 v83, 0x45800000, v82
	v_cndmask_b32_e32 v82, v82, v83, vcc
	v_pk_mul_f32 v[66:67], v[82:83], v[66:67] op_sel_hi:[0,1]
	v_pk_mul_f32 v[70:71], v[82:83], v[70:71] op_sel_hi:[0,1]
	v_pk_mul_f32 v[64:65], v[82:83], v[64:65] op_sel_hi:[0,1]
	v_pk_mul_f32 v[66:67], v[8:9], v[66:67]
	v_pk_mul_f32 v[68:69], v[82:83], v[68:69] op_sel_hi:[0,1]
	v_pk_mul_f32 v[70:71], v[34:35], v[70:71]
	v_pk_mul_f32 v[64:65], v[10:11], v[64:65]
	v_pk_mul_f32 v[68:69], v[6:7], v[68:69]
	v_bfe_u32 v82, v71, 16, 1
	v_bfe_u32 v83, v70, 16, 1
	v_bfe_u32 v84, v67, 16, 1
	v_bfe_u32 v85, v66, 16, 1
	v_add3_u32 v85, v66, v85, s27
	v_add3_u32 v84, v67, v84, s27
	v_add3_u32 v66, v70, v83, s27
	v_add3_u32 v67, v71, v82, s27
	v_bfe_u32 v70, v64, 16, 1
	v_bfe_u32 v71, v65, 16, 1
	v_bfe_u32 v82, v68, 16, 1
	v_bfe_u32 v83, v69, 16, 1
	v_add3_u32 v69, v69, v83, s27
	v_add3_u32 v68, v68, v82, s27
	v_add3_u32 v65, v65, v71, s27
	v_add3_u32 v64, v64, v70, s27
	v_lshrrev_b32_e32 v64, 16, v64
	v_lshrrev_b32_e32 v65, 16, v65
	v_lshrrev_b32_e32 v68, 16, v68
	v_lshrrev_b32_e32 v69, 16, v69
	v_and_or_b32 v67, v67, s9, v69
	v_and_or_b32 v66, v66, s9, v68
	v_and_or_b32 v65, v84, s9, v65
	v_and_or_b32 v64, v85, s9, v64
	v_lshl_add_u64 v[68:69], s[90:91], 0, v[46:47]
	global_store_dwordx4 v[68:69], v[64:67], off
	s_or_b64 exec, exec, s[22:23]
	s_and_saveexec_b64 s[22:23], s[4:5]
	s_cbranch_execnz .LBB0_2787
